# grid barriers: acquire-side L1 invalidate issued before the spin (followers) and after the XCC generation bump (leader); plus relaxed false vmcnt waits in DSA steps
# speedup vs baseline: 1.2541x; 1.0016x over previous
.LBB0_1019:
	v_readlane_b32 s14, v250, 31
	v_readlane_b32 s15, v250, 32
	v_cvt_f32_u32_e32 v0, v3
	v_sub_u32_e32 v5, 0, v3
	v_rcp_iflag_f32_e32 v0, v0
	s_nop 1
	global_atomic_add v4, v1, v225, s[14:15] sc0
	v_mul_f32_e32 v0, 0x4f7ffffe, v0
	v_cvt_u32_f32_e32 v0, v0
	v_mul_lo_u32 v5, v5, v0
	v_mul_hi_u32 v5, v0, v5
	v_add_u32_e32 v0, v0, v5
	s_waitcnt vmcnt(0)
	v_mul_hi_u32 v0, v4, v0
	v_mul_lo_u32 v5, v0, v3
	v_sub_u32_e32 v5, v4, v5
	v_add_u32_e32 v6, 1, v0
	v_cmp_ge_u32_e32 vcc, v5, v3
	v_add_u32_e32 v4, 1, v4
	s_nop 0
	v_cndmask_b32_e32 v0, v0, v6, vcc
	v_sub_u32_e32 v6, v5, v3
	v_cndmask_b32_e32 v5, v5, v6, vcc
	v_add_u32_e32 v6, 1, v0
	v_cmp_ge_u32_e32 vcc, v5, v3
	s_nop 1
	v_cndmask_b32_e32 v0, v0, v6, vcc
	v_mul_lo_u32 v5, v3, v0
	v_add_u32_e32 v3, v5, v3
	v_cmp_ne_u32_e32 vcc, v4, v3
	s_and_saveexec_b64 s[14:15], vcc
	s_xor_b64 s[14:15], exec, s[14:15]
	s_cbranch_execz .LBB0_1033
	v_readlane_b32 s16, v250, 33
	v_readlane_b32 s17, v250, 34
	s_waitcnt lgkmcnt(0)
	s_nop 3
	buffer_inv sc1
	global_load_dword v2, v1, s[16:17] sc1
	s_waitcnt vmcnt(0)
	v_cmp_eq_u32_e32 vcc, v2, v0
	s_and_saveexec_b64 s[16:17], vcc
	s_cbranch_execz .LBB0_1032
	s_mov_b32 s29, 1
	s_mov_b64 s[30:31], 0
	s_branch .LBB0_1023

.LBB0_1032:
	s_or_b64 exec, exec, s[16:17]
	s_waitcnt vmcnt(0)
	s_waitcnt vmcnt(0)
.LBB0_1033:
	s_andn2_saveexec_b64 s[14:15], s[14:15]
	s_mov_b32 s101, 0
	s_cbranch_execz .LBB0_2078
	s_mov_b64 s[14:15], exec
	buffer_wbl2 sc1
	s_waitcnt lgkmcnt(0)
	s_waitcnt vmcnt(0)
	v_mbcnt_lo_u32_b32 v0, s14, 0
	v_mbcnt_hi_u32_b32 v0, s15, v0
	v_cmp_eq_u32_e32 vcc, 0, v0
	s_and_saveexec_b64 s[16:17], vcc
	s_cbranch_execz .LBB0_1036
	s_bcnt1_i32_b64 s14, s[14:15]
	v_mov_b32_e32 v3, s14
	v_readlane_b32 s14, v251, 37
	v_readlane_b32 s15, v251, 38
	s_nop 4
	global_atomic_add v3, v1, v3, s[14:15] sc0
.LBB0_1036:
	s_or_b64 exec, exec, s[16:17]
	s_waitcnt vmcnt(0)
	v_readfirstlane_b32 s14, v3
	v_sub_u32_e32 v4, 0, v2
	s_mov_b64 s[16:17], -1
	v_add_u32_e32 v3, s14, v0
	v_cvt_f32_u32_e32 v0, v2
	v_readlane_b32 s14, v251, 39
	v_readlane_b32 s15, v251, 40
	v_rcp_iflag_f32_e32 v0, v0
	s_nop 0
	v_mul_f32_e32 v0, 0x4f7ffffe, v0
	v_cvt_u32_f32_e32 v0, v0
	v_mul_lo_u32 v4, v4, v0
	v_mul_hi_u32 v4, v0, v4
	v_add_u32_e32 v0, v0, v4
	v_mul_hi_u32 v0, v3, v0
	v_mul_lo_u32 v4, v0, v2
	v_sub_u32_e32 v4, v3, v4
	v_cmp_ge_u32_e32 vcc, v4, v2
	v_add_u32_e32 v5, 1, v0
	v_add_u32_e32 v3, 1, v3
	v_cndmask_b32_e32 v0, v0, v5, vcc
	v_sub_u32_e32 v5, v4, v2
	v_cndmask_b32_e32 v4, v4, v5, vcc
	v_cmp_ge_u32_e32 vcc, v4, v2
	v_add_u32_e32 v4, 1, v0
	s_nop 0
	v_cndmask_b32_e32 v0, v0, v4, vcc
	v_mul_lo_u32 v4, v2, v0
	v_add_u32_e32 v2, v4, v2
	v_cmp_ne_u32_e32 vcc, v3, v2
	v_mov_b64_e32 v[2:3], s[14:15]
	s_and_saveexec_b64 s[14:15], vcc
	s_cbranch_execz .LBB0_2075
	v_readlane_b32 s16, v251, 39
	v_readlane_b32 s17, v251, 40
	s_mov_b64 s[30:31], 0
	s_nop 3
	buffer_inv sc1
	s_mov_b32 s101, 1
	global_load_dword v2, v1, s[16:17] sc1
	s_waitcnt vmcnt(0)
	v_cmp_eq_u32_e32 vcc, v2, v0
	s_and_saveexec_b64 s[16:17], vcc
	s_cbranch_execz .LBB0_2074
	s_mov_b32 s29, 1
	s_branch .LBB0_1040

.LBB0_1075:
	s_waitcnt vmcnt(0) lgkmcnt(0)
	s_barrier
	v_exp_f32_e32 v48, v2
	v_exp_f32_e32 v49, v3
	v_lshl_add_u64 v[2:3], v[216:217], 0, s[70:71]
	s_mov_b32 s38, m0
	s_mov_b32 m0, s63
	s_nop 0
	global_load_lds_dwordx4 v[2:3], off
	s_mov_b32 m0, s38
	v_lshl_add_u64 v[2:3], v[218:219], 0, s[12:13]
	s_add_i32 s38, s63, 0x8000
	s_mov_b32 s39, m0
	s_mov_b32 m0, s38
	s_nop 0
	global_load_lds_dwordx4 v[2:3], off
	s_mov_b32 m0, s39
	ds_read_b128 v[172:175], v241 offset:8192
	ds_read_b128 v[164:167], v241 offset:8704
	ds_read_b128 v[168:171], v241 offset:10240
	ds_read_b128 v[160:163], v241 offset:10752
	ds_read_b128 v[156:159], v241 offset:12288
	ds_read_b128 v[152:155], v241 offset:12800
	ds_read_b128 v[148:151], v241 offset:14336
	ds_read_b128 v[144:147], v241 offset:14848
	v_exp_f32_e32 v64, v37
	v_exp_f32_e32 v65, v18
	v_exp_f32_e32 v66, v19
	v_exp_f32_e32 v67, v20
	v_exp_f32_e32 v68, v21
	v_exp_f32_e32 v69, v22
	v_exp_f32_e32 v70, v23
	v_exp_f32_e32 v71, v24
	v_exp_f32_e32 v72, v25
	v_exp_f32_e32 v73, v26
	v_exp_f32_e32 v74, v27
	v_exp_f32_e32 v75, v28
	v_exp_f32_e32 v76, v29
	v_exp_f32_e32 v77, v30
	v_exp_f32_e32 v78, v31
	v_exp_f32_e32 v79, v32
	v_exp_f32_e32 v50, v4
	v_exp_f32_e32 v51, v5
	v_exp_f32_e32 v52, v6
	v_exp_f32_e32 v53, v7
	v_exp_f32_e32 v54, v8
	v_exp_f32_e32 v55, v9
	v_exp_f32_e32 v56, v10
	v_exp_f32_e32 v57, v11
	v_exp_f32_e32 v58, v12
	v_exp_f32_e32 v59, v13
	v_exp_f32_e32 v60, v14
	v_exp_f32_e32 v61, v15
	v_exp_f32_e32 v62, v16
	v_exp_f32_e32 v63, v17
	s_and_b32 s29, s41, 0x3fffffc0
	s_addk_i32 s42, 0x100
	s_waitcnt vmcnt(2) lgkmcnt(0)
	s_barrier
	s_lshl_b32 s29, s29, 2
	s_lshr_b32 s64, s42, 6
	v_or_b32_e32 v0, v36, v0
	v_cmp_ne_u32_e64 s[42:43], 0, v0
	s_cmp_eq_u32 s40, 0
	v_lshl_add_u32 v205, v236, 2, s29
	v_lshl_add_u32 v203, v238, 2, s29
	v_lshl_add_u64 v[220:221], v[34:35], 2, s[48:49]
	s_cbranch_scc1 .LBB0_1151
	v_mov_b32_e32 v14, v1
	v_mov_b32_e32 v15, v1
	v_lshl_add_u64 v[184:185], v[34:35], 2, s[48:49]
	v_mov_b32_e32 v0, v1
	v_mov_b32_e32 v2, v1
	v_mov_b32_e32 v3, v1
	v_mov_b32_e32 v4, v1
	v_mov_b32_e32 v5, v1
	v_mov_b32_e32 v6, v1
	v_mov_b32_e32 v7, v1
	v_mov_b32_e32 v8, v1
	v_mov_b32_e32 v9, v1
	v_mov_b32_e32 v10, v1
	v_mov_b32_e32 v11, v1
	v_mov_b32_e32 v12, v1
	v_mov_b32_e32 v13, v1
	v_mov_b64_e32 v[46:47], v[14:15]
	v_mov_b64_e32 v[30:31], v[14:15]
	v_lshl_add_u64 v[182:183], v[180:181], 2, s[46:47]
	s_mov_b32 s29, 0
	s_movk_i32 s57, 0x4000
	s_movk_i32 s59, 0x2000
	v_mov_b32_e32 v248, 0
	s_mov_b32 s58, 6
	s_mov_b64 s[54:55], 0
	v_mov_b64_e32 v[44:45], v[12:13]
	v_mov_b64_e32 v[42:43], v[10:11]
	v_mov_b64_e32 v[40:41], v[8:9]
	v_mov_b64_e32 v[38:39], v[6:7]
	v_mov_b64_e32 v[36:37], v[4:5]
	v_mov_b64_e32 v[34:35], v[2:3]
	v_mov_b64_e32 v[32:33], v[0:1]
	v_mov_b64_e32 v[28:29], v[12:13]
	v_mov_b64_e32 v[26:27], v[10:11]
	v_mov_b64_e32 v[24:25], v[8:9]
	v_mov_b64_e32 v[22:23], v[6:7]
	v_mov_b64_e32 v[20:21], v[4:5]
	v_mov_b64_e32 v[18:19], v[2:3]
	v_mov_b64_e32 v[16:17], v[0:1]
.LBB0_1077:
	v_lshl_add_u64 v[14:15], v[184:185], 0, s[54:55]
	s_mov_b32 s38, 0xeb20000
	v_add_co_u32_e32 v2, vcc, s38, v14
	s_mov_b32 s38, 0xeb28000
	s_nop 0
	v_addc_co_u32_e32 v3, vcc, 0, v15, vcc
	v_add_co_u32_e32 v4, vcc, s38, v14
	v_add_u32_e32 v12, s29, v239
	s_nop 0
	v_addc_co_u32_e32 v5, vcc, 0, v15, vcc
	global_load_dword v0, v[2:3], off
	global_load_dword v190, v[4:5], off
	global_load_dword v191, v[182:183], off offset:-4
	ds_read_b64_tr_b16 v[176:177], v12 offset:24576
	ds_read_b64_tr_b16 v[178:179], v12 offset:25088
	s_waitcnt lgkmcnt(9)
	v_mfma_f32_32x32x16_bf16 v[80:95], v[172:175], v[124:127], 0
	v_add_f32_e32 v2, v64, v65
	v_add_f32_e32 v2, v66, v2
	v_add_f32_e32 v2, v67, v2
	v_add_f32_e32 v2, v68, v2
	v_add_f32_e32 v2, v69, v2
	v_cvt_pk_bf16_f32 v140, v64, v65
	v_cvt_pk_bf16_f32 v141, v66, v67
	ds_read_b64_tr_b16 v[172:173], v12 offset:28672
	ds_read_b64_tr_b16 v[174:175], v12 offset:29184
	s_waitcnt lgkmcnt(10)
	v_mfma_f32_32x32x16_bf16 v[96:111], v[164:167], v[124:127], 0
	v_add_f32_e32 v2, v70, v2
	v_add_f32_e32 v2, v71, v2
	v_add_f32_e32 v2, v72, v2
	v_add_f32_e32 v2, v73, v2
	v_cvt_pk_bf16_f32 v142, v68, v69
	v_cvt_pk_bf16_f32 v143, v70, v71
	ds_read_b64_tr_b16 v[164:165], v12 offset:25600
	ds_read_b64_tr_b16 v[166:167], v12 offset:26112
	s_waitcnt lgkmcnt(11)
	v_mfma_f32_32x32x16_bf16 v[80:95], v[168:171], v[120:123], v[80:95]
	v_add_f32_e32 v2, v74, v2
	v_add_f32_e32 v2, v75, v2
	v_add_f32_e32 v2, v76, v2
	v_add_f32_e32 v2, v77, v2
	v_cvt_pk_bf16_f32 v136, v72, v73
	v_cvt_pk_bf16_f32 v137, v74, v75
	ds_read_b64_tr_b16 v[168:169], v12 offset:29696
	ds_read_b64_tr_b16 v[170:171], v12 offset:30208
	s_waitcnt lgkmcnt(12)
	v_mfma_f32_32x32x16_bf16 v[96:111], v[160:163], v[120:123], v[96:111]
	v_add_f32_e32 v2, v78, v2
	v_add_f32_e32 v2, v79, v2
	v_add_f32_e32 v2, v48, v2
	v_add_f32_e32 v2, v49, v2
	v_cvt_pk_bf16_f32 v138, v76, v77
	v_cvt_pk_bf16_f32 v139, v78, v79
	ds_read_b64_tr_b16 v[160:161], v12 offset:26624
	ds_read_b64_tr_b16 v[162:163], v12 offset:27136
	s_waitcnt lgkmcnt(13)
	v_mfma_f32_32x32x16_bf16 v[80:95], v[156:159], v[116:119], v[80:95]
	v_add_f32_e32 v2, v50, v2
	v_add_f32_e32 v2, v51, v2
	v_add_f32_e32 v2, v52, v2
	v_add_f32_e32 v6, v53, v2
	v_cvt_pk_bf16_f32 v132, v48, v49
	v_cvt_pk_bf16_f32 v133, v50, v51
	ds_read_b64_tr_b16 v[2:3], v12 offset:30720
	ds_read_b64_tr_b16 v[4:5], v12 offset:31232
	s_waitcnt lgkmcnt(14)
	v_mfma_f32_32x32x16_bf16 v[96:111], v[152:155], v[116:119], v[96:111]
	v_add_f32_e32 v6, v54, v6
	v_add_f32_e32 v6, v55, v6
	v_add_f32_e32 v6, v56, v6
	v_add_f32_e32 v10, v57, v6
	v_cvt_pk_bf16_f32 v134, v52, v53
	v_cvt_pk_bf16_f32 v135, v54, v55
	ds_read_b64_tr_b16 v[6:7], v12 offset:27648
	ds_read_b64_tr_b16 v[8:9], v12 offset:28160
	s_waitcnt lgkmcnt(14)
	v_mfma_f32_32x32x16_bf16 v[80:95], v[148:151], v[112:115], v[80:95]
	v_add_f32_e32 v10, v58, v10
	v_add_f32_e32 v10, v59, v10
	v_add_f32_e32 v10, v60, v10
	v_add_f32_e32 v48, v61, v10
	v_cvt_pk_bf16_f32 v128, v56, v57
	v_cvt_pk_bf16_f32 v129, v58, v59
	ds_read_b64_tr_b16 v[10:11], v12 offset:31744
	ds_read_b64_tr_b16 v[12:13], v12 offset:32256
	v_mfma_f32_32x32x16_bf16 v[96:111], v[144:147], v[112:115], v[96:111]
	v_add_f32_e32 v48, v62, v48
	v_add_f32_e32 v48, v63, v48
	v_add_f32_e32 v48, 0, v48
	v_cvt_pk_bf16_f32 v130, v60, v61
	v_cvt_pk_bf16_f32 v131, v62, v63
	v_lshl_add_u64 v[186:187], v[216:217], 0, s[54:55]
	v_lshl_add_u64 v[50:51], v[186:187], 0, s[20:21]
	s_add_i32 s29, s59, s63
	s_mov_b32 s38, m0
	s_mov_b32 m0, s29
	s_nop 0
	global_load_lds_dwordx4 v[50:51], off
	s_mov_b32 m0, s38
	v_lshl_add_u64 v[188:189], v[218:219], 0, s[54:55]
	v_lshl_add_u64 v[50:51], v[188:189], 0, s[24:25]
	s_add_i32 s29, s57, s62
	s_mov_b32 s38, m0
	s_mov_b32 m0, s29
	s_nop 0
	global_load_lds_dwordx4 v[50:51], off
	s_mov_b32 m0, s38
	s_waitcnt vmcnt(7)
	v_mul_f32_e32 v49, v201, v209
	v_cmp_nge_f32_e32 vcc, s73, v49
	v_cmp_neq_f32_e64 s[38:39], 0, v207
	s_or_b64 vcc, vcc, s[38:39]
	v_cndmask_b32_e64 v49, 0, 1, vcc
	v_cmp_ne_u32_e64 s[38:39], 0, v49
	s_cmp_lg_u64 s[38:39], 0
	s_cselect_b64 s[38:39], -1, 0
	s_cbranch_vccz .LBB0_1079
	v_sub_f32_e32 v95, v95, v207
	v_sub_f32_e32 v94, v94, v207
	v_sub_f32_e32 v93, v93, v207
	v_sub_f32_e32 v92, v92, v207
	v_sub_f32_e32 v91, v91, v207
	v_sub_f32_e32 v90, v90, v207
	v_sub_f32_e32 v89, v89, v207
	v_sub_f32_e32 v88, v88, v207
	v_sub_f32_e32 v87, v87, v207
	v_sub_f32_e32 v86, v86, v207
	v_sub_f32_e32 v85, v85, v207
	v_sub_f32_e32 v84, v84, v207
	v_sub_f32_e32 v83, v83, v207
	v_sub_f32_e32 v82, v82, v207
	v_sub_f32_e32 v81, v81, v207
	v_sub_f32_e32 v80, v80, v207
	v_sub_f32_e32 v111, v111, v207
	v_sub_f32_e32 v110, v110, v207
	v_sub_f32_e32 v109, v109, v207
	v_sub_f32_e32 v108, v108, v207
	v_sub_f32_e32 v107, v107, v207
	v_sub_f32_e32 v106, v106, v207
	v_sub_f32_e32 v105, v105, v207
	v_sub_f32_e32 v104, v104, v207
	v_sub_f32_e32 v103, v103, v207
	v_sub_f32_e32 v102, v102, v207
	v_sub_f32_e32 v101, v101, v207
	v_sub_f32_e32 v100, v100, v207
	v_sub_f32_e32 v99, v99, v207
	v_sub_f32_e32 v98, v98, v207
	v_sub_f32_e32 v97, v97, v207
	v_sub_f32_e32 v96, v96, v207

.LBB0_2077:
	s_or_b64 exec, exec, s[14:15]
	v_readlane_b32 s14, v250, 33
	v_readlane_b32 s15, v250, 34
	s_waitcnt vmcnt(0)
	s_nop 3
	global_atomic_add v1, v225, s[14:15]
	s_cmp_eq_u32 s101, 1
	s_cbranch_scc1 .Lxb_lead_inv_done
	buffer_inv sc1
.Lxb_lead_inv_done:
	s_waitcnt vmcnt(0)
.LBB0_2078:
	s_or_b64 exec, exec, s[0:1]
	s_waitcnt lgkmcnt(0)
	s_barrier
	s_branch .LBB0_2096
.LBB0_2079:
	s_mov_b32 s101, 0
	s_mov_b32 s0, -1
	s_waitcnt vmcnt(0)
	s_waitcnt vmcnt(0) lgkmcnt(0)
	v_mbcnt_lo_u32_b32 v0, s0, 0
	v_mbcnt_hi_u32_b32 v0, s0, v0
	v_readlane_b32 s0, v250, 30
	s_barrier
	s_nop 0
	v_cmp_eq_u32_e32 vcc, s0, v0
	s_and_saveexec_b64 s[0:1], vcc
	s_cbranch_execz .LBB0_2095
	v_readlane_b32 s14, v250, 8
	s_waitcnt vmcnt(0) expcnt(0) lgkmcnt(0)
	s_mov_b64 s[16:17], -1
	v_mov_b32_e32 v0, s14
	v_readlane_b32 s14, v250, 31
	v_readlane_b32 s15, v250, 32
	ds_read_b32 v2, v0
	s_waitcnt lgkmcnt(0)
	v_cvt_f32_u32_e32 v0, v2
	s_nop 1
	global_atomic_add v3, v1, v225, s[14:15] sc0
	v_sub_u32_e32 v4, 0, v2
	v_readlane_b32 s14, v250, 33
	v_rcp_iflag_f32_e32 v0, v0
	v_readlane_b32 s15, v250, 34
	v_mul_f32_e32 v0, 0x4f7ffffe, v0
	v_cvt_u32_f32_e32 v0, v0
	v_mul_lo_u32 v4, v4, v0
	v_mul_hi_u32 v4, v0, v4
	v_add_u32_e32 v0, v0, v4
	s_waitcnt vmcnt(0)
	v_mul_hi_u32 v0, v3, v0
	v_mul_lo_u32 v4, v0, v2
	v_sub_u32_e32 v4, v3, v4
	v_cmp_ge_u32_e32 vcc, v4, v2
	v_add_u32_e32 v5, 1, v0
	v_add_u32_e32 v3, 1, v3
	v_cndmask_b32_e32 v0, v0, v5, vcc
	v_sub_u32_e32 v5, v4, v2
	v_cndmask_b32_e32 v4, v4, v5, vcc
	v_cmp_ge_u32_e32 vcc, v4, v2
	v_add_u32_e32 v4, 1, v0
	s_nop 0
	v_cndmask_b32_e32 v0, v0, v4, vcc
	v_mul_lo_u32 v4, v2, v0
	v_add_u32_e32 v2, v4, v2
	v_cmp_ne_u32_e32 vcc, v3, v2
	v_mov_b64_e32 v[2:3], s[14:15]
	s_and_saveexec_b64 s[14:15], vcc
	s_cbranch_execz .LBB0_2092
	v_readlane_b32 s16, v250, 33
	v_readlane_b32 s17, v250, 34
	s_mov_b64 s[30:31], 0
	s_nop 3
	buffer_inv sc1
	s_mov_b32 s101, 1
	global_load_dword v2, v1, s[16:17] sc1
	s_waitcnt vmcnt(0)
	v_cmp_eq_u32_e32 vcc, v2, v0
	s_and_saveexec_b64 s[16:17], vcc
	s_cbranch_execz .LBB0_2091
	s_mov_b32 s29, 1
	s_branch .LBB0_2084

.LBB0_2094:
	s_or_b64 exec, exec, s[14:15]
	s_waitcnt vmcnt(0)
	s_cmp_eq_u32 s101, 1
	s_cbranch_scc1 .Lxb_loc_inv_done
	buffer_inv sc1
.Lxb_loc_inv_done:
	s_waitcnt vmcnt(0)
.LBB0_2095:
	s_or_b64 exec, exec, s[0:1]
	s_barrier

	.amdhsa_kernel _Z6mk_fwd4Args
		.amdhsa_group_segment_fixed_size 147456
		.amdhsa_private_segment_fixed_size 0
		.amdhsa_kernarg_size 440
		.amdhsa_user_sgpr_count 2
		.amdhsa_user_sgpr_dispatch_ptr 0
		.amdhsa_user_sgpr_queue_ptr 0
		.amdhsa_user_sgpr_kernarg_segment_ptr 1
		.amdhsa_user_sgpr_dispatch_id 0
		.amdhsa_user_sgpr_kernarg_preload_length 0
		.amdhsa_user_sgpr_kernarg_preload_offset 0
		.amdhsa_user_sgpr_private_segment_size 0
		.amdhsa_uses_dynamic_stack 0
		.amdhsa_enable_private_segment 0
		.amdhsa_system_sgpr_workgroup_id_x 1
		.amdhsa_system_sgpr_workgroup_id_y 0
		.amdhsa_system_sgpr_workgroup_id_z 0
		.amdhsa_system_sgpr_workgroup_info 0
		.amdhsa_system_vgpr_workitem_id 0
		.amdhsa_next_free_vgpr 256
		.amdhsa_next_free_sgpr 102
		.amdhsa_accum_offset 256
		.amdhsa_reserve_vcc 1
		.amdhsa_float_round_mode_32 0
		.amdhsa_float_round_mode_16_64 0
		.amdhsa_float_denorm_mode_32 3
		.amdhsa_float_denorm_mode_16_64 3
		.amdhsa_dx10_clamp 1
		.amdhsa_ieee_mode 1
		.amdhsa_fp16_overflow 0
		.amdhsa_tg_split 0
		.amdhsa_exception_fp_ieee_invalid_op 0
		.amdhsa_exception_fp_denorm_src 0
		.amdhsa_exception_fp_ieee_div_zero 0
		.amdhsa_exception_fp_ieee_overflow 0
		.amdhsa_exception_fp_ieee_underflow 0
		.amdhsa_exception_fp_ieee_inexact 0
		.amdhsa_exception_int_div_zero 0
	.end_amdhsa_kernel

amdhsa.kernels:
  - .agpr_count:     0
    .args:
      - .offset:         0
        .size:           184
        .value_kind:     by_value
      - .offset:         184
        .size:           4
        .value_kind:     hidden_block_count_x
      - .offset:         188
        .size:           4
        .value_kind:     hidden_block_count_y
      - .offset:         192
        .size:           4
        .value_kind:     hidden_block_count_z
      - .offset:         196
        .size:           2
        .value_kind:     hidden_group_size_x
      - .offset:         198
        .size:           2
        .value_kind:     hidden_group_size_y
      - .offset:         200
        .size:           2
        .value_kind:     hidden_group_size_z
      - .offset:         202
        .size:           2
        .value_kind:     hidden_remainder_x
      - .offset:         204
        .size:           2
        .value_kind:     hidden_remainder_y
      - .offset:         206
        .size:           2
        .value_kind:     hidden_remainder_z
      - .offset:         224
        .size:           8
        .value_kind:     hidden_global_offset_x
      - .offset:         232
        .size:           8
        .value_kind:     hidden_global_offset_y
      - .offset:         240
        .size:           8
        .value_kind:     hidden_global_offset_z
      - .offset:         248
        .size:           2
        .value_kind:     hidden_grid_dims
    .group_segment_fixed_size: 147456
    .kernarg_segment_align: 8
    .kernarg_segment_size: 440
    .language:       OpenCL C
    .language_version:
      - 2
      - 0
    .max_flat_workgroup_size: 512
    .name:           _Z6mk_fwd4Args
    .private_segment_fixed_size: 0
    .sgpr_count:     108
    .sgpr_spill_count: 415
    .symbol:         _Z6mk_fwd4Args.kd
    .uniform_work_group_size: 1
    .uses_dynamic_stack: false
    .vgpr_count:     256
    .vgpr_spill_count: 0
    .wavefront_size: 64
